# GEMM_IN: removed the compiler's full vmcnt(0) drain at each unit start (the template's counted waits already cover the staged tiles; epilogue stores now drain under the first phases)
# baseline (speedup 1.0000x reference)
.LBB0_301:
	s_add_u32 s0, s2, 0x100
	s_addc_u32 s1, s3, 0
	s_add_u32 s52, s18, 0x100
	s_addc_u32 s53, s19, 0
	s_add_u32 s2, s2, 0x80
	s_addc_u32 s3, s3, 0
	s_mov_b32 s87, -2
	s_cmp_eq_u32 s87, 12
	s_cselect_b32 s14, s48, s0
	s_cselect_b32 s15, s49, s1
	s_cselect_b32 s18, s50, s52
	s_cselect_b32 s19, s51, s53
	s_add_u32 s28, s14, 0x80
	s_addc_u32 s29, s15, 0
	s_add_i32 s90, 0, 0x10000
	v_add_u32_e32 v144, s90, v35
	ds_read_b128 v[132:135], v144
	ds_read_b128 v[136:139], v144 offset:1024
	ds_read_b128 v[140:143], v144 offset:2048
	ds_read_b128 v[144:147], v144 offset:3072
	s_mov_b64 s[88:89], s[2:3]
	ds_read_b128 v[160:163], v172
	ds_read_b128 v[164:167], v172 offset:1024
	ds_read_b128 v[174:177], v172 offset:2048
	ds_read_b128 v[178:181], v172 offset:3072
	ds_read_b128 v[182:185], v172 offset:4096
	ds_read_b128 v[186:189], v172 offset:5120
	ds_read_b128 v[190:193], v172 offset:6144
	ds_read_b128 v[194:197], v172 offset:7168
	s_add_i32 m0, s71, 0xc000
	v_lshl_add_u64 v[168:169], s[88:89], 0, v[156:157]
	global_load_lds_dwordx4 v[168:169], off
	v_lshl_add_u64 v[168:169], s[88:89], 0, v[158:159]
	s_add_i32 m0, s71, 0xe000
	s_nop 0
	global_load_lds_dwordx4 v[168:169], off
	s_waitcnt lgkmcnt(8)
	s_barrier
	s_waitcnt lgkmcnt(0)
	s_setprio 1
	s_waitcnt lgkmcnt(0)
	v_mfma_f32_16x16x32_bf16 v[128:131], v[132:135], v[160:163], 0
	v_mfma_f32_16x16x32_bf16 v[124:127], v[140:143], v[160:163], 0
	v_mfma_f32_16x16x32_bf16 v[120:123], v[132:135], v[174:177], 0
	v_mfma_f32_16x16x32_bf16 v[116:119], v[140:143], v[174:177], 0
	v_mfma_f32_16x16x32_bf16 v[104:107], v[132:135], v[182:185], 0
	v_mfma_f32_16x16x32_bf16 v[100:103], v[140:143], v[182:185], 0
	v_mfma_f32_16x16x32_bf16 v[88:91], v[132:135], v[190:193], 0
	v_mfma_f32_16x16x32_bf16 v[84:87], v[140:143], v[190:193], 0
	v_mfma_f32_16x16x32_bf16 v[128:131], v[136:139], v[164:167], v[128:131]
	v_mfma_f32_16x16x32_bf16 v[124:127], v[144:147], v[164:167], v[124:127]
	v_mfma_f32_16x16x32_bf16 v[120:123], v[136:139], v[178:181], v[120:123]
	v_mfma_f32_16x16x32_bf16 v[116:119], v[144:147], v[178:181], v[116:119]
	v_mfma_f32_16x16x32_bf16 v[104:107], v[136:139], v[186:189], v[104:107]
	v_mfma_f32_16x16x32_bf16 v[100:103], v[144:147], v[186:189], v[100:103]
	v_mfma_f32_16x16x32_bf16 v[88:91], v[136:139], v[194:197], v[88:91]
	v_mfma_f32_16x16x32_bf16 v[84:87], v[144:147], v[194:197], v[84:87]
	s_setprio 0
	s_barrier
	s_add_i32 s91, 0, 0x14000
	v_add_u32_e32 v168, s91, v35
	s_mov_b64 s[88:89], s[18:19]
	s_add_i32 s90, s90, s58
	ds_read_b128 v[198:201], v168
	ds_read_b128 v[202:205], v168 offset:1024
	ds_read_b128 v[206:209], v168 offset:2048
	ds_read_b128 v[218:221], v168 offset:3072
	s_mov_b32 m0, s90
	v_lshl_add_u64 v[168:169], s[88:89], 0, v[150:151]
	global_load_lds_dwordx4 v[168:169], off
	v_lshl_add_u64 v[168:169], s[88:89], 0, v[148:149]
	s_add_i32 m0, s90, 0x2000
	s_nop 0
	global_load_lds_dwordx4 v[168:169], off
	s_barrier
	s_waitcnt lgkmcnt(0)
	s_setprio 1
	s_waitcnt lgkmcnt(0)
	v_mfma_f32_16x16x32_bf16 v[112:115], v[198:201], v[160:163], 0
	v_mfma_f32_16x16x32_bf16 v[108:111], v[206:209], v[160:163], 0
	v_mfma_f32_16x16x32_bf16 v[96:99], v[198:201], v[174:177], 0
	v_mfma_f32_16x16x32_bf16 v[92:95], v[206:209], v[174:177], 0
	v_mfma_f32_16x16x32_bf16 v[80:83], v[198:201], v[182:185], 0
	v_mfma_f32_16x16x32_bf16 v[76:79], v[206:209], v[182:185], 0
	v_mfma_f32_16x16x32_bf16 v[72:75], v[198:201], v[190:193], 0
	v_mfma_f32_16x16x32_bf16 v[68:71], v[206:209], v[190:193], 0
	v_mfma_f32_16x16x32_bf16 v[112:115], v[202:205], v[164:167], v[112:115]
	v_mfma_f32_16x16x32_bf16 v[108:111], v[218:221], v[164:167], v[108:111]
	v_mfma_f32_16x16x32_bf16 v[96:99], v[202:205], v[178:181], v[96:99]
	v_mfma_f32_16x16x32_bf16 v[92:95], v[218:221], v[178:181], v[92:95]
	v_mfma_f32_16x16x32_bf16 v[80:83], v[202:205], v[186:189], v[80:83]
	v_mfma_f32_16x16x32_bf16 v[76:79], v[218:221], v[186:189], v[76:79]
	v_mfma_f32_16x16x32_bf16 v[72:75], v[202:205], v[194:197], v[72:75]
	v_mfma_f32_16x16x32_bf16 v[68:71], v[218:221], v[194:197], v[68:71]
	s_setprio 0
	s_mov_b64 s[88:89], s[14:15]
	s_mov_b32 m0, s71
	s_barrier
	ds_read_b128 v[160:163], v172 offset:16384
	ds_read_b128 v[164:167], v172 offset:17408
	ds_read_b128 v[174:177], v172 offset:18432
	ds_read_b128 v[178:181], v172 offset:19456
	ds_read_b128 v[182:185], v172 offset:20480
	ds_read_b128 v[186:189], v172 offset:21504
	ds_read_b128 v[190:193], v172 offset:22528
	ds_read_b128 v[194:197], v172 offset:23552
	s_nop 0
	v_lshl_add_u64 v[168:169], s[88:89], 0, v[152:153]
	global_load_lds_dwordx4 v[168:169], off
	v_lshl_add_u64 v[168:169], s[88:89], 0, v[154:155]
	s_mov_b32 m0, s37
	s_nop 0
	global_load_lds_dwordx4 v[168:169], off
	s_barrier
	s_waitcnt lgkmcnt(0)
	s_setprio 1
	s_waitcnt lgkmcnt(0)
	v_mfma_f32_16x16x32_bf16 v[64:67], v[132:135], v[160:163], 0
	v_mfma_f32_16x16x32_bf16 v[60:63], v[140:143], v[160:163], 0
	v_mfma_f32_16x16x32_bf16 v[56:59], v[132:135], v[174:177], 0
	v_mfma_f32_16x16x32_bf16 v[52:55], v[140:143], v[174:177], 0
	v_mfma_f32_16x16x32_bf16 v[40:43], v[132:135], v[182:185], 0
	v_mfma_f32_16x16x32_bf16 v[36:39], v[140:143], v[182:185], 0
	v_mfma_f32_16x16x32_bf16 v[22:25], v[132:135], v[190:193], 0
	v_mfma_f32_16x16x32_bf16 v[18:21], v[140:143], v[190:193], 0
	v_mfma_f32_16x16x32_bf16 v[64:67], v[136:139], v[164:167], v[64:67]
	v_mfma_f32_16x16x32_bf16 v[60:63], v[144:147], v[164:167], v[60:63]
	v_mfma_f32_16x16x32_bf16 v[56:59], v[136:139], v[178:181], v[56:59]
	v_mfma_f32_16x16x32_bf16 v[52:55], v[144:147], v[178:181], v[52:55]
	v_mfma_f32_16x16x32_bf16 v[40:43], v[136:139], v[186:189], v[40:43]
	v_mfma_f32_16x16x32_bf16 v[36:39], v[144:147], v[186:189], v[36:39]
	v_mfma_f32_16x16x32_bf16 v[22:25], v[136:139], v[194:197], v[22:25]
	v_mfma_f32_16x16x32_bf16 v[18:21], v[144:147], v[194:197], v[18:21]
	s_setprio 0
	s_barrier
	s_add_u32 s88, s18, 0x40000
	s_addc_u32 s89, s19, 0
	s_add_i32 s90, s91, s58
	s_mov_b32 m0, s90
	v_lshl_add_u64 v[132:133], s[88:89], 0, v[150:151]
	global_load_lds_dwordx4 v[132:133], off
	v_lshl_add_u64 v[132:133], s[88:89], 0, v[148:149]
	s_add_i32 m0, s90, 0x2000
	s_nop 0
	global_load_lds_dwordx4 v[132:133], off
	s_waitcnt vmcnt(6)
	s_barrier
	s_setprio 1
	v_mfma_f32_16x16x32_bf16 v[48:51], v[198:201], v[160:163], 0
	v_mfma_f32_16x16x32_bf16 v[44:47], v[206:209], v[160:163], 0
	v_mfma_f32_16x16x32_bf16 v[30:33], v[198:201], v[174:177], 0
	v_mfma_f32_16x16x32_bf16 v[26:29], v[206:209], v[174:177], 0
	v_mfma_f32_16x16x32_bf16 v[14:17], v[198:201], v[182:185], 0
	v_mfma_f32_16x16x32_bf16 v[10:13], v[206:209], v[182:185], 0
	v_mfma_f32_16x16x32_bf16 v[6:9], v[198:201], v[190:193], 0
	v_mfma_f32_16x16x32_bf16 v[2:5], v[206:209], v[190:193], 0
	v_mfma_f32_16x16x32_bf16 v[48:51], v[202:205], v[164:167], v[48:51]
	v_mfma_f32_16x16x32_bf16 v[44:47], v[218:221], v[164:167], v[44:47]
	v_mfma_f32_16x16x32_bf16 v[30:33], v[202:205], v[178:181], v[30:33]
	v_mfma_f32_16x16x32_bf16 v[26:29], v[218:221], v[178:181], v[26:29]
	v_mfma_f32_16x16x32_bf16 v[14:17], v[202:205], v[186:189], v[14:17]
	v_mfma_f32_16x16x32_bf16 v[10:13], v[218:221], v[186:189], v[10:13]
	v_mfma_f32_16x16x32_bf16 v[6:9], v[202:205], v[194:197], v[6:9]
	v_mfma_f32_16x16x32_bf16 v[2:5], v[218:221], v[194:197], v[2:5]
	s_setprio 0
	s_add_i32 s88, 0, 0x18000
	v_add_u32_e32 v144, s88, v35
	s_barrier
	ds_read_b128 v[132:135], v144
	ds_read_b128 v[136:139], v144 offset:1024
	ds_read_b128 v[140:143], v144 offset:2048
	ds_read_b128 v[144:147], v144 offset:3072
	s_mov_b32 m0, s76
	ds_read_b128 v[160:163], v172 offset:32768
	ds_read_b128 v[164:167], v172 offset:33792
	ds_read_b128 v[174:177], v172 offset:34816
	ds_read_b128 v[178:181], v172 offset:35840
	ds_read_b128 v[182:185], v172 offset:36864
	ds_read_b128 v[186:189], v172 offset:37888
	ds_read_b128 v[190:193], v172 offset:38912
	ds_read_b128 v[194:197], v172 offset:39936
	s_nop 0
	v_lshl_add_u64 v[168:169], s[14:15], 0, v[156:157]
	global_load_lds_dwordx4 v[168:169], off
	v_lshl_add_u64 v[168:169], s[14:15], 0, v[158:159]
	s_mov_b32 m0, s77
	s_nop 0
	global_load_lds_dwordx4 v[168:169], off
	s_waitcnt lgkmcnt(8)
	s_barrier
	s_waitcnt lgkmcnt(0)
	s_setprio 1
	s_waitcnt lgkmcnt(0)
	v_mfma_f32_16x16x32_bf16 v[128:131], v[132:135], v[160:163], v[128:131]
	v_mfma_f32_16x16x32_bf16 v[124:127], v[140:143], v[160:163], v[124:127]
	v_mfma_f32_16x16x32_bf16 v[120:123], v[132:135], v[174:177], v[120:123]
	v_mfma_f32_16x16x32_bf16 v[116:119], v[140:143], v[174:177], v[116:119]
	v_mfma_f32_16x16x32_bf16 v[104:107], v[132:135], v[182:185], v[104:107]
	v_mfma_f32_16x16x32_bf16 v[100:103], v[140:143], v[182:185], v[100:103]
	v_mfma_f32_16x16x32_bf16 v[88:91], v[132:135], v[190:193], v[88:91]
	v_mfma_f32_16x16x32_bf16 v[84:87], v[140:143], v[190:193], v[84:87]
	v_mfma_f32_16x16x32_bf16 v[128:131], v[136:139], v[164:167], v[128:131]
	v_mfma_f32_16x16x32_bf16 v[124:127], v[144:147], v[164:167], v[124:127]
	v_mfma_f32_16x16x32_bf16 v[120:123], v[136:139], v[178:181], v[120:123]
	v_mfma_f32_16x16x32_bf16 v[116:119], v[144:147], v[178:181], v[116:119]
	v_mfma_f32_16x16x32_bf16 v[104:107], v[136:139], v[186:189], v[104:107]
	v_mfma_f32_16x16x32_bf16 v[100:103], v[144:147], v[186:189], v[100:103]
	v_mfma_f32_16x16x32_bf16 v[88:91], v[136:139], v[194:197], v[88:91]
	v_mfma_f32_16x16x32_bf16 v[84:87], v[144:147], v[194:197], v[84:87]
	s_setprio 0
	s_barrier
	s_add_i32 s89, 0, 0x1c000
	s_add_u32 s14, s18, 0x80
	v_add_u32_e32 v168, s89, v35
	s_addc_u32 s15, s19, 0
	s_add_i32 s88, s88, s58
	ds_read_b128 v[198:201], v168
	ds_read_b128 v[202:205], v168 offset:1024
	ds_read_b128 v[206:209], v168 offset:2048
	ds_read_b128 v[218:221], v168 offset:3072
	s_mov_b32 m0, s88
	v_lshl_add_u64 v[168:169], s[14:15], 0, v[150:151]
	global_load_lds_dwordx4 v[168:169], off
	v_lshl_add_u64 v[168:169], s[14:15], 0, v[148:149]
	s_add_i32 m0, s88, 0x2000
	s_nop 0
	global_load_lds_dwordx4 v[168:169], off
	s_barrier
	s_waitcnt lgkmcnt(0)
	s_setprio 1
	s_waitcnt lgkmcnt(0)
	v_mfma_f32_16x16x32_bf16 v[112:115], v[198:201], v[160:163], v[112:115]
	v_mfma_f32_16x16x32_bf16 v[108:111], v[206:209], v[160:163], v[108:111]
	v_mfma_f32_16x16x32_bf16 v[96:99], v[198:201], v[174:177], v[96:99]
	v_mfma_f32_16x16x32_bf16 v[92:95], v[206:209], v[174:177], v[92:95]
	v_mfma_f32_16x16x32_bf16 v[80:83], v[198:201], v[182:185], v[80:83]
	v_mfma_f32_16x16x32_bf16 v[76:79], v[206:209], v[182:185], v[76:79]
	v_mfma_f32_16x16x32_bf16 v[72:75], v[198:201], v[190:193], v[72:75]
	v_mfma_f32_16x16x32_bf16 v[68:71], v[206:209], v[190:193], v[68:71]
	v_mfma_f32_16x16x32_bf16 v[112:115], v[202:205], v[164:167], v[112:115]
	v_mfma_f32_16x16x32_bf16 v[108:111], v[218:221], v[164:167], v[108:111]
	v_mfma_f32_16x16x32_bf16 v[96:99], v[202:205], v[178:181], v[96:99]
	v_mfma_f32_16x16x32_bf16 v[92:95], v[218:221], v[178:181], v[92:95]
	v_mfma_f32_16x16x32_bf16 v[80:83], v[202:205], v[186:189], v[80:83]
	v_mfma_f32_16x16x32_bf16 v[76:79], v[218:221], v[186:189], v[76:79]
	v_mfma_f32_16x16x32_bf16 v[72:75], v[202:205], v[194:197], v[72:75]
	v_mfma_f32_16x16x32_bf16 v[68:71], v[218:221], v[194:197], v[68:71]
	s_setprio 0
	s_mov_b32 m0, s80
	s_barrier
	ds_read_b128 v[160:163], v172 offset:49152
	ds_read_b128 v[164:167], v172 offset:50176
	ds_read_b128 v[174:177], v172 offset:51200
	ds_read_b128 v[178:181], v172 offset:52224
	ds_read_b128 v[182:185], v172 offset:53248
	ds_read_b128 v[186:189], v172 offset:54272
	ds_read_b128 v[190:193], v172 offset:55296
	ds_read_b128 v[194:197], v172 offset:56320
	s_nop 0
	v_lshl_add_u64 v[168:169], s[28:29], 0, v[152:153]
	global_load_lds_dwordx4 v[168:169], off
	v_lshl_add_u64 v[168:169], s[28:29], 0, v[154:155]
	s_mov_b32 m0, s81
	s_nop 0
	global_load_lds_dwordx4 v[168:169], off
	s_barrier
	s_waitcnt lgkmcnt(0)
	s_setprio 1
	s_waitcnt lgkmcnt(0)
	v_mfma_f32_16x16x32_bf16 v[64:67], v[132:135], v[160:163], v[64:67]
	v_mfma_f32_16x16x32_bf16 v[60:63], v[140:143], v[160:163], v[60:63]
	v_mfma_f32_16x16x32_bf16 v[56:59], v[132:135], v[174:177], v[56:59]
	v_mfma_f32_16x16x32_bf16 v[52:55], v[140:143], v[174:177], v[52:55]
	v_mfma_f32_16x16x32_bf16 v[40:43], v[132:135], v[182:185], v[40:43]
	v_mfma_f32_16x16x32_bf16 v[36:39], v[140:143], v[182:185], v[36:39]
	v_mfma_f32_16x16x32_bf16 v[22:25], v[132:135], v[190:193], v[22:25]
	v_mfma_f32_16x16x32_bf16 v[18:21], v[140:143], v[190:193], v[18:21]
	v_mfma_f32_16x16x32_bf16 v[64:67], v[136:139], v[164:167], v[64:67]
	v_mfma_f32_16x16x32_bf16 v[60:63], v[144:147], v[164:167], v[60:63]
	v_mfma_f32_16x16x32_bf16 v[56:59], v[136:139], v[178:181], v[56:59]
	v_mfma_f32_16x16x32_bf16 v[52:55], v[144:147], v[178:181], v[52:55]
	v_mfma_f32_16x16x32_bf16 v[40:43], v[136:139], v[186:189], v[40:43]
	v_mfma_f32_16x16x32_bf16 v[36:39], v[144:147], v[186:189], v[36:39]
	v_mfma_f32_16x16x32_bf16 v[22:25], v[136:139], v[194:197], v[22:25]
	v_mfma_f32_16x16x32_bf16 v[18:21], v[144:147], v[194:197], v[18:21]
	s_setprio 0
	s_barrier
	s_add_u32 s14, s18, 0x40080
	s_addc_u32 s15, s19, 0
	s_add_i32 s18, s89, s58
	s_mov_b32 m0, s18
	v_lshl_add_u64 v[132:133], s[14:15], 0, v[150:151]
	global_load_lds_dwordx4 v[132:133], off
	v_lshl_add_u64 v[132:133], s[14:15], 0, v[148:149]
	s_add_i32 m0, s18, 0x2000
	s_nop 0
	global_load_lds_dwordx4 v[132:133], off
	s_waitcnt vmcnt(6)
	s_barrier
	s_setprio 1
	v_mfma_f32_16x16x32_bf16 v[48:51], v[198:201], v[160:163], v[48:51]
	v_mfma_f32_16x16x32_bf16 v[44:47], v[206:209], v[160:163], v[44:47]
	v_mfma_f32_16x16x32_bf16 v[30:33], v[198:201], v[174:177], v[30:33]
	v_mfma_f32_16x16x32_bf16 v[26:29], v[206:209], v[174:177], v[26:29]
	v_mfma_f32_16x16x32_bf16 v[14:17], v[198:201], v[182:185], v[14:17]
	v_mfma_f32_16x16x32_bf16 v[10:13], v[206:209], v[182:185], v[10:13]
	v_mfma_f32_16x16x32_bf16 v[6:9], v[198:201], v[190:193], v[6:9]
	v_mfma_f32_16x16x32_bf16 v[2:5], v[206:209], v[190:193], v[2:5]
	v_mfma_f32_16x16x32_bf16 v[48:51], v[202:205], v[164:167], v[48:51]
	v_mfma_f32_16x16x32_bf16 v[44:47], v[218:221], v[164:167], v[44:47]
	v_mfma_f32_16x16x32_bf16 v[30:33], v[202:205], v[178:181], v[30:33]
	v_mfma_f32_16x16x32_bf16 v[26:29], v[218:221], v[178:181], v[26:29]
	v_mfma_f32_16x16x32_bf16 v[14:17], v[202:205], v[186:189], v[14:17]
	v_mfma_f32_16x16x32_bf16 v[10:13], v[218:221], v[186:189], v[10:13]
	v_mfma_f32_16x16x32_bf16 v[6:9], v[202:205], v[194:197], v[6:9]
	v_mfma_f32_16x16x32_bf16 v[2:5], v[218:221], v[194:197], v[2:5]
	s_setprio 0
	s_add_i32 s87, s87, 2
	s_add_u32 s0, s0, 0x100
	s_addc_u32 s1, s1, 0
	s_add_u32 s52, s52, 0x100
	s_addc_u32 s53, s53, 0
	s_add_u32 s2, s2, 0x100
	s_addc_u32 s3, s3, 0
	s_cmp_gt_u32 s87, 13
	s_barrier
	s_cbranch_scc0 .LBB0_302
	s_branch .Lpeel_exit_0
